# NSA unit: gated-combine operand loads requested in the unit prologue (picked up by moves), queue barrier no longer waits for previous unit's store acks
# speedup vs baseline: 1.0019x; 1.0019x over previous
.LBB0_633:
	v_readlane_b32 s48, v253, 1
	v_readlane_b32 s49, v253, 2
	s_load_dword s0, s[48:49], 0xd8
	v_readlane_b32 s2, v254, 5
	v_readlane_b32 s3, v254, 6
	s_xor_b64 s[2:3], s[2:3], -1
	v_writelane_b32 v254, s2, 13
	s_add_i32 s1, s66, 2
	s_waitcnt lgkmcnt(0)
	s_cmp_lt_i32 s1, s0
	v_writelane_b32 v254, s3, 14
	v_writelane_b32 v254, s66, 15
	s_cbranch_scc1 .LBB0_894
	s_load_dword s0, s[48:49], 0xdc
	s_waitcnt lgkmcnt(0)
	v_writelane_b32 v254, s0, 16
	s_cmp_gt_i32 s1, s0
	s_cbranch_scc1 .LBB0_894
	s_load_dwordx2 s[2:3], s[48:49], 0xd0
	v_writelane_b32 v254, s1, 17
	s_nop 0
	v_readlane_b32 s0, v254, 7
	v_readlane_b32 s1, v254, 8
	s_lshl_b32 s82, s0, 9
	s_lshl_b64 s[0:1], s[82:83], 2
	s_waitcnt lgkmcnt(0)
	s_add_u32 s0, s2, s0
	s_addc_u32 s1, s3, s1
	v_writelane_b32 v254, s0, 18
	s_add_u32 s0, s0, 0x4400
	v_writelane_b32 v254, s1, 19
	s_addc_u32 s1, s1, 0
	s_add_u32 s50, s2, 0x26ac2000
	v_writelane_b32 v254, s0, 20
	s_addc_u32 s51, s3, 0
	s_nop 0
	v_writelane_b32 v254, s1, 21
	s_add_u32 s0, s2, 0x49ac2000
	v_writelane_b32 v254, s0, 22
	s_addc_u32 s0, s3, 0
	v_writelane_b32 v254, s0, 23
	s_add_u32 s0, s2, 0x47ac2000
	s_addc_u32 s1, s3, 0
	v_writelane_b32 v254, s0, 24
	s_nop 1
	v_writelane_b32 v254, s1, 25
	s_add_u32 s0, s2, 0x43ac2000
	s_addc_u32 s1, s3, 0
	v_writelane_b32 v254, s0, 26
	s_nop 1
	v_writelane_b32 v254, s1, 27
	s_add_u32 s0, s2, 0x1aaa2000
	v_writelane_b32 v254, s0, 28
	s_addc_u32 s0, s3, 0
	v_writelane_b32 v254, s0, 29
	s_add_u32 s0, s2, 0x1a6a2000
	v_writelane_b32 v254, s0, 30
	s_addc_u32 s0, s3, 0
	v_writelane_b32 v254, s0, 31
	s_add_u32 s0, s2, 0x22a2000
	v_writelane_b32 v254, s0, 32
	s_addc_u32 s0, s3, 0
	v_writelane_b32 v254, s0, 33
	s_add_u32 s0, s2, 0x1ca2000
	v_writelane_b32 v254, s0, 34
	s_addc_u32 s0, s3, 0
	v_writelane_b32 v254, s0, 35
	s_add_u32 s0, s2, 0x862000
	v_writelane_b32 v254, s0, 36
	v_writelane_b32 v254, s2, 37
	s_addc_u32 s0, s3, 0
	s_nop 0
	v_writelane_b32 v254, s3, 38
	v_writelane_b32 v254, s0, 39
	v_writelane_b32 v254, s48, 40
	s_nop 1
	v_writelane_b32 v254, s49, 41
	v_writelane_b32 v254, s50, 42
	s_nop 1
	v_writelane_b32 v254, s51, 43
	v_cmp_eq_u32_e32 vcc, 0, v0
	s_and_saveexec_b64 s[84:85], vcc
	s_cbranch_execz .Lnsa_tk_skip
	v_readlane_b32 s86, v254, 20
	v_readlane_b32 s87, v254, 21
	v_mov_b32_e32 v251, 1
	s_nop 3
	global_atomic_add v251, v3, v251, s[86:87] sc0
	s_waitcnt vmcnt(0)

.LBB0_638:
	s_setprio 0
	v_mov_b32_e32 v2, v0
	s_barrier
	s_nop 0
	v_cmp_eq_u32_e32 vcc, 0, v2
	s_and_saveexec_b64 s[0:1], vcc
	s_cbranch_execz .LBB0_642
	v_mov_b32_e32 v4, s73
	ds_write_b32 v4, v251
	v_readlane_b32 s4, v254, 20
	v_readlane_b32 s5, v254, 21
	v_mov_b32_e32 v251, 1
	s_nop 3
	global_atomic_add v251, v3, v251, s[4:5] sc0

.LBB0_645:
	s_ashr_i32 s18, s12, 5
	s_sub_i32 s6, 31, s18
	s_ashr_i32 s0, s0, 3
	s_lshl_b32 s3, s6, 6
	s_and_b32 s19, s0, 0xffffffe0
	v_and_b32_e32 v129, 31, v65
	s_add_i32 s14, s19, s3
	s_bfe_u32 s5, s12, 0x40001
	v_or_b32_e32 v126, s14, v129
	s_and_b32 s4, s12, 1
	s_lshl_b32 s82, s5, 11
	v_ashrrev_i32_e32 v127, 31, v126
	s_and_b32 s2, s1, 3
	s_lshl_b32 s1, s4, 2
	v_lshl_add_u64 v[122:123], s[82:83], 0, v[126:127]
	v_mov_b64_e32 v[4:5], s[50:51]
	s_or_b32 s13, s2, s1
	v_mad_u64_u32 v[124:125], s[0:1], v122, s70, v[4:5]
	v_bfe_u32 v68, v65, 5, 1
	v_mad_i32_i24 v125, v123, s70, v125
	s_lshl_b32 s82, s13, 7
	v_lshl_add_u64 v[4:5], v[124:125], 0, s[82:83]
	v_lshlrev_b32_e32 v2, 4, v68
	v_lshl_add_u64 v[4:5], v[4:5], 0, v[2:3]
	s_mov_b64 s[0:1], 0x1200
	v_lshl_add_u64 v[6:7], v[4:5], 0, s[0:1]
	s_movk_i32 s0, 0x1000
	v_add_co_u32_e32 v4, vcc, s0, v4
	v_bfe_u32 v2, v65, 4, 5
	s_nop 0
	v_addc_co_u32_e32 v5, vcc, 0, v5, vcc
	global_load_dwordx4 v[98:101], v[6:7], off offset:32
	global_load_dwordx4 v[102:105], v[6:7], off offset:64
	global_load_dwordx4 v[106:109], v[4:5], off offset:512
	global_load_dwordx4 v[110:113], v[6:7], off offset:96
	s_mul_i32 s84, s13, 6
	s_mov_b32 s85, 0
	v_readlane_b32 s86, v254, 24
	v_readlane_b32 s87, v254, 25
	v_lshl_add_u64 v[234:235], v[124:125], 0, s[84:85]
	s_mov_b64 s[84:85], 0x3400
	v_lshl_add_u64 v[234:235], v[234:235], 0, s[84:85]
	v_lshlrev_b64 v[236:237], 10, v[122:123]
	global_load_dword v250, v[234:235], off
	global_load_ushort v221, v[234:235], off offset:4
	v_lshl_add_u64 v[234:235], s[86:87], 0, v[236:237]
	s_lshl_b32 s84, s13, 7
	s_mov_b32 s85, 0
	v_lshlrev_b32_e32 v236, 3, v68
	v_mov_b32_e32 v237, 0
	v_lshl_add_u64 v[234:235], v[234:235], 0, s[84:85]
	v_lshl_add_u64 v[234:235], v[234:235], 0, v[236:237]
	global_load_dwordx2 v[236:237], v[234:235], off
	global_load_dwordx2 v[238:239], v[234:235], off offset:16
	global_load_dwordx2 v[240:241], v[234:235], off offset:32
	global_load_dwordx2 v[242:243], v[234:235], off offset:48
	global_load_dwordx2 v[244:245], v[234:235], off offset:64
	global_load_dwordx2 v[246:247], v[234:235], off offset:80
	global_load_dwordx2 v[248:249], v[234:235], off offset:96
	global_load_dwordx2 v[234:235], v[234:235], off offset:112
	v_bitop3_b32 v4, v65, v2, s74 bitop3:0x6c
	s_lshl_b32 s7, s5, 15
	v_readlane_b32 s9, v254, 22
	v_lshlrev_b32_e32 v2, 1, v2
	v_lshrrev_b32_e32 v5, 3, v4
	s_add_u32 s0, s9, s7
	v_readlane_b32 s10, v254, 23
	v_and_or_b32 v2, v5, 1, v2
	v_ashrrev_i32_e32 v5, 2, v65
	s_addc_u32 s1, s10, 0
	s_lshl_b32 s8, s4, 14
	v_and_b32_e32 v5, 0xffffff80, v5
	v_lshlrev_b32_e32 v4, 4, v4
	s_add_u32 s0, s0, s8
	v_and_or_b32 v4, v4, s72, v5
	v_bfe_i32 v6, v65, 4, 24
	v_bfe_u32 v5, v65, 3, 1
	s_addc_u32 s1, s1, 0
	s_or_b32 s7, s7, s8
	v_lshl_or_b32 v5, v6, 1, v5
	v_lshlrev_b32_e32 v6, 2, v6
	s_add_u32 s7, s9, s7
	v_lshlrev_b32_e32 v66, 4, v65
	v_xor_b32_e32 v6, v6, v65
	v_and_b32_e32 v7, 3, v65
	s_addc_u32 s10, s10, 0
	v_lshl_add_u32 v4, v2, 7, v4
	v_and_or_b32 v6, v6, 4, v7
	v_add_u32_e32 v127, 0, v66
	s_add_u32 s8, s7, 0x80000
	v_lshlrev_b32_e32 v6, 4, v6
	v_mov_b32_e32 v8, v4
	v_readfirstlane_b32 s11, v127
	s_addc_u32 s9, s10, 0
	v_lshl_or_b32 v7, v5, 7, v6
	s_mov_b32 m0, s11
	v_add_u32_e32 v64, 0x2000, v127
	global_load_lds_dwordx4 v8, s[0:1]
	v_mov_b32_e32 v8, v7
	v_readfirstlane_b32 s11, v64
	s_add_u32 s0, s0, 0x2000
	s_mov_b32 m0, s11
	s_addc_u32 s1, s1, 0
	v_add_u32_e32 v9, 0x4000, v127
	global_load_lds_dwordx4 v8, s[8:9]
	s_add_u32 s8, s7, 0x82000
	v_mov_b32_e32 v8, v4
	v_readfirstlane_b32 s7, v9
	s_mov_b32 m0, s7
	s_addc_u32 s9, s10, 0
	global_load_lds_dwordx4 v8, s[0:1]
	v_add_u32_e32 v8, 0x6000, v127
	v_cmp_eq_u32_e32 vcc, 0, v65
	v_readfirstlane_b32 s0, v8
	s_mov_b32 m0, s0
	s_nop 0
	global_load_lds_dwordx4 v7, s[8:9]
	s_and_saveexec_b64 s[0:1], vcc
	s_movk_i32 s10, 0x84
	s_cbranch_execz .LBB0_647
	v_readlane_b32 s7, v254, 0
	s_nop 1
	v_mov_b32_e32 v7, s7
	ds_write_b32 v7, v3

.LBB0_698:
	s_mul_i32 s0, s15, 6
	s_mov_b32 s1, s83
	v_lshl_add_u64 v[4:5], v[124:125], 0, s[0:1]
	s_mov_b64 s[0:1], 0x3400
	v_lshl_add_u64 v[6:7], v[4:5], 0, s[0:1]
	v_add_co_u32_e32 v4, vcc, 0x3000, v4
	v_readlane_b32 s0, v254, 24
	s_nop 0
	v_addc_co_u32_e32 v5, vcc, 0, v5, vcc
	v_mov_b32_e32 v5, v250
	v_mov_b32_e32 v4, v144
	s_nop 1
	v_permlane32_swap_b32_e32 v144, v4
	v_add_f32_e32 v10, v144, v4
	v_mov_b32_e32 v4, v221
	v_lshlrev_b64 v[8:9], 10, v[122:123]
	v_readlane_b32 s1, v254, 25
	v_mov_b32_e32 v129, v3
	v_lshlrev_b64 v[6:7], 9, v[122:123]
	v_lshl_add_u64 v[8:9], s[0:1], 0, v[8:9]
	s_lshl_b32 s0, s82, 1
	s_mov_b32 s1, s83
	v_lshl_add_u64 v[8:9], v[8:9], 0, s[0:1]
	v_lshl_add_u64 v[8:9], v[128:129], 1, v[8:9]
	v_mov_b64_e32 v[88:89], v[236:237]
	v_mov_b64_e32 v[86:87], v[238:239]
	v_mov_b64_e32 v[84:85], v[240:241]
	v_mov_b64_e32 v[82:83], v[242:243]
	v_mov_b64_e32 v[16:17], v[244:245]
	v_mov_b64_e32 v[14:15], v[246:247]
	v_mov_b64_e32 v[12:13], v[248:249]
	s_nop 0
	v_mov_b64_e32 v[8:9], v[234:235]
	s_cmpk_gt_i32 s14, 0x25f
	v_readlane_b32 s2, v254, 13
	v_readlane_b32 s3, v254, 14
	s_waitcnt vmcnt(0)
	v_and_b32_e32 v2, 0xffff0000, v5
	v_div_scale_f32 v11, s[0:1], v10, v10, v2
	v_rcp_f32_e32 v90, v11
	v_readlane_b32 s0, v254, 26
	v_lshlrev_b32_e32 v4, 16, v4
	v_readlane_b32 s1, v254, 27
	v_fma_f32 v91, -v11, v90, 1.0
	v_fmac_f32_e32 v90, v91, v90
	v_div_scale_f32 v91, vcc, v2, v10, v2
	v_mul_f32_e32 v92, v91, v90
	v_fma_f32 v93, -v11, v92, v91
	v_fmac_f32_e32 v92, v93, v90
	v_fma_f32 v11, -v11, v92, v91
	v_div_fmas_f32 v11, v11, v90, v92
	v_div_fixup_f32 v2, v11, v10, v2
	v_lshlrev_b32_e32 v11, 16, v5
	v_lshlrev_b32_e32 v90, 16, v88
	v_mov_b32_e32 v5, v34
	v_mov_b32_e32 v91, v11
	v_pk_mul_f32 v[90:91], v[4:5], v[90:91]
	v_and_b32_e32 v92, 0xffff0000, v88
	v_fma_f32 v5, v66, v2, v91
	v_add_f32_e32 v66, v90, v5
	v_mov_b32_e32 v5, v35
	v_mov_b32_e32 v93, v11
	v_pk_mul_f32 v[34:35], v[4:5], v[92:93]
	v_lshlrev_b32_e32 v10, 16, v89
	v_fma_f32 v5, v67, v2, v35
	v_add_f32_e32 v67, v34, v5
	v_mov_b32_e32 v5, v36
	v_pk_mul_f32 v[34:35], v[4:5], v[10:11]
	v_and_b32_e32 v10, 0xffff0000, v89
	v_fma_f32 v5, v68, v2, v35
	v_add_f32_e32 v36, v34, v5
	v_mov_b32_e32 v5, v37
	v_pk_mul_f32 v[34:35], v[4:5], v[10:11]
	v_mul_f32_e32 v10, 0x41800000, v66
	v_fma_f32 v5, v69, v2, v35
	v_add_f32_e32 v5, v34, v5
	v_mul_f32_e32 v34, 0x41800000, v67
	v_med3_f32 v35, v34, s78, v198
	v_mul_f32_e32 v34, 0x41800000, v36
	v_med3_f32 v10, v10, s78, v198
	v_med3_f32 v36, v34, s78, v198
	v_mov_b32_e32 v34, v3
	v_cvt_pk_fp8_f32 v34, v10, v35
	v_mul_f32_e32 v5, 0x41800000, v5
	v_med3_f32 v5, v5, s78, v198
	v_lshlrev_b32_e32 v37, 16, v86
	v_cvt_pk_fp8_f32 v34, v36, v5 op_sel:[0,0,1]
	v_mov_b32_e32 v66, v38
	v_mov_b32_e32 v67, v4
	v_mov_b32_e32 v36, v11
	v_pk_mul_f32 v[36:37], v[66:67], v[36:37]
	v_mov_b32_e32 v38, v39
	v_fma_f32 v5, v70, v2, v36
	v_add_f32_e32 v5, v5, v37
	v_and_b32_e32 v37, 0xffff0000, v86
	v_mov_b32_e32 v39, v4
	v_mov_b32_e32 v36, v11
	v_pk_mul_f32 v[36:37], v[38:39], v[36:37]
	v_mov_b32_e32 v38, v40
	v_fma_f32 v10, v71, v2, v36
	v_add_f32_e32 v10, v10, v37
	v_lshlrev_b32_e32 v37, 16, v87
	v_mov_b32_e32 v36, v11
	v_pk_mul_f32 v[36:37], v[38:39], v[36:37]
	v_mov_b32_e32 v38, v41
	v_fma_f32 v35, v72, v2, v36
	v_add_f32_e32 v35, v35, v37
	v_and_b32_e32 v37, 0xffff0000, v87
	v_mov_b32_e32 v36, v11
	v_pk_mul_f32 v[36:37], v[38:39], v[36:37]
	v_mul_f32_e32 v35, 0x41800000, v35
	v_fma_f32 v36, v73, v2, v36
	v_add_f32_e32 v36, v36, v37
	v_mul_f32_e32 v5, 0x41800000, v5
	v_mul_f32_e32 v10, 0x41800000, v10
	v_med3_f32 v37, v35, s78, v198
	v_mul_f32_e32 v35, 0x41800000, v36
	v_med3_f32 v5, v5, s78, v198
	v_med3_f32 v10, v10, s78, v198
	v_med3_f32 v36, v35, s78, v198
	v_mov_b32_e32 v35, v3
	v_cvt_pk_fp8_f32 v35, v5, v10
	v_lshl_add_u64 v[6:7], s[0:1], 0, v[6:7]
	v_lshl_add_u64 v[6:7], v[6:7], 0, s[82:83]
	v_lshl_add_u64 v[6:7], v[6:7], 0, v[130:131]
	v_cvt_pk_fp8_f32 v35, v37, v36 op_sel:[0,0,1]
	v_mov_b32_e32 v36, v42
	v_mov_b32_e32 v37, v4
	s_cselect_b64 s[0:1], -1, 0
	v_permlane32_swap_b32_e32 v34, v35
	global_store_dwordx2 v[6:7], v[34:35], off
	v_lshlrev_b32_e32 v35, 16, v84
	v_mov_b32_e32 v34, v11
	v_pk_mul_f32 v[34:35], v[36:37], v[34:35]
	v_mov_b32_e32 v36, v43
	v_fma_f32 v5, v74, v2, v34
	v_add_f32_e32 v5, v5, v35
	v_and_b32_e32 v35, 0xffff0000, v84
	v_mov_b32_e32 v34, v11
	v_pk_mul_f32 v[34:35], v[36:37], v[34:35]
	v_mov_b32_e32 v36, v44
	v_fma_f32 v10, v75, v2, v34
	v_add_f32_e32 v10, v10, v35
	v_lshlrev_b32_e32 v35, 16, v85
	v_mov_b32_e32 v34, v11
	v_pk_mul_f32 v[34:35], v[36:37], v[34:35]
	v_mov_b32_e32 v36, v45
	v_fma_f32 v34, v76, v2, v34
	v_add_f32_e32 v38, v34, v35
	v_and_b32_e32 v35, 0xffff0000, v85
	v_mov_b32_e32 v34, v11
	v_pk_mul_f32 v[34:35], v[36:37], v[34:35]
	v_mul_f32_e32 v5, 0x41800000, v5
	v_fma_f32 v34, v77, v2, v34
	v_add_f32_e32 v34, v34, v35
	v_mul_f32_e32 v10, 0x41800000, v10
	v_mul_f32_e32 v34, 0x41800000, v34
	v_med3_f32 v5, v5, s78, v198
	v_med3_f32 v10, v10, s78, v198
	v_med3_f32 v36, v34, s78, v198
	v_mov_b32_e32 v34, v3
	v_cvt_pk_fp8_f32 v34, v5, v10
	v_mul_f32_e32 v35, 0x41800000, v38
	v_med3_f32 v35, v35, s78, v198
	v_lshlrev_b32_e32 v37, 16, v82
	v_cvt_pk_fp8_f32 v34, v35, v36 op_sel:[0,0,1]
	v_mov_b32_e32 v38, v46
	v_mov_b32_e32 v36, v11
	v_pk_mul_f32 v[36:37], v[38:39], v[36:37]
	v_mov_b32_e32 v38, v47
	v_fma_f32 v5, v78, v2, v36
	v_add_f32_e32 v5, v5, v37
	v_and_b32_e32 v37, 0xffff0000, v82
	v_mov_b32_e32 v36, v11
	v_pk_mul_f32 v[36:37], v[38:39], v[36:37]
	v_mov_b32_e32 v38, v48
	v_fma_f32 v10, v79, v2, v36
	v_add_f32_e32 v10, v10, v37
	v_lshlrev_b32_e32 v37, 16, v83
	v_mov_b32_e32 v36, v11
	v_pk_mul_f32 v[36:37], v[38:39], v[36:37]
	v_mov_b32_e32 v38, v49
	v_fma_f32 v35, v80, v2, v36
	v_add_f32_e32 v35, v35, v37
	v_and_b32_e32 v37, 0xffff0000, v83
	v_mov_b32_e32 v36, v11
	v_pk_mul_f32 v[36:37], v[38:39], v[36:37]
	v_mul_f32_e32 v35, 0x41800000, v35
	v_fma_f32 v36, v81, v2, v36
	v_add_f32_e32 v36, v36, v37
	v_mul_f32_e32 v5, 0x41800000, v5
	v_mul_f32_e32 v10, 0x41800000, v10
	v_med3_f32 v37, v35, s78, v198
	v_mul_f32_e32 v35, 0x41800000, v36
	v_med3_f32 v5, v5, s78, v198
	v_med3_f32 v10, v10, s78, v198
	v_med3_f32 v36, v35, s78, v198
	v_mov_b32_e32 v35, v3
	v_cvt_pk_fp8_f32 v35, v5, v10
	s_or_b64 s[0:1], s[2:3], s[0:1]
	s_and_b64 vcc, exec, s[0:1]
	v_cvt_pk_fp8_f32 v35, v37, v36 op_sel:[0,0,1]
	v_mov_b32_e32 v36, v18
	v_mov_b32_e32 v37, v4
	v_mov_b32_e32 v18, v19
	v_permlane32_swap_b32_e32 v34, v35
	global_store_dwordx2 v[6:7], v[34:35], off offset:16
	v_lshlrev_b32_e32 v35, 16, v16
	v_mov_b32_e32 v34, v11
	v_pk_mul_f32 v[34:35], v[36:37], v[34:35]
	v_mov_b32_e32 v19, v4
	v_fma_f32 v5, v50, v2, v34
	v_add_f32_e32 v5, v5, v35
	v_and_b32_e32 v35, 0xffff0000, v16
	v_mov_b32_e32 v34, v11
	v_pk_mul_f32 v[18:19], v[18:19], v[34:35]
	v_mov_b32_e32 v34, v20
	v_fma_f32 v10, v51, v2, v18
	v_add_f32_e32 v10, v10, v19
	v_lshlrev_b32_e32 v19, 16, v17
	v_mov_b32_e32 v35, v4
	v_mov_b32_e32 v18, v11
	v_pk_mul_f32 v[18:19], v[34:35], v[18:19]
	v_and_b32_e32 v17, 0xffff0000, v17
	v_fma_f32 v16, v52, v2, v18
	v_add_f32_e32 v20, v16, v19
	v_mov_b32_e32 v18, v21
	v_mov_b32_e32 v19, v4
	v_mov_b32_e32 v16, v11
	v_pk_mul_f32 v[16:17], v[18:19], v[16:17]
	v_mul_f32_e32 v5, 0x41800000, v5
	v_fma_f32 v16, v53, v2, v16
	v_add_f32_e32 v16, v16, v17
	v_mul_f32_e32 v10, 0x41800000, v10
	v_mul_f32_e32 v16, 0x41800000, v16
	v_med3_f32 v5, v5, s78, v198
	v_med3_f32 v10, v10, s78, v198
	v_med3_f32 v18, v16, s78, v198
	v_mov_b32_e32 v16, v3
	v_cvt_pk_fp8_f32 v16, v5, v10
	v_mul_f32_e32 v17, 0x41800000, v20
	v_med3_f32 v17, v17, s78, v198
	v_lshlrev_b32_e32 v19, 16, v14
	v_cvt_pk_fp8_f32 v16, v17, v18 op_sel:[0,0,1]
	v_mov_b32_e32 v20, v22
	v_mov_b32_e32 v21, v4
	v_mov_b32_e32 v18, v11
	v_pk_mul_f32 v[18:19], v[20:21], v[18:19]
	v_mov_b32_e32 v20, v23
	v_fma_f32 v5, v54, v2, v18
	v_add_f32_e32 v5, v5, v19
	v_and_b32_e32 v19, 0xffff0000, v14
	v_mov_b32_e32 v18, v11
	v_pk_mul_f32 v[18:19], v[20:21], v[18:19]
	v_mov_b32_e32 v20, v24
	v_fma_f32 v10, v55, v2, v18
	v_add_f32_e32 v10, v10, v19
	v_lshlrev_b32_e32 v19, 16, v15
	v_mov_b32_e32 v18, v11
	v_pk_mul_f32 v[18:19], v[20:21], v[18:19]
	v_and_b32_e32 v15, 0xffff0000, v15
	v_fma_f32 v14, v56, v2, v18
	v_add_f32_e32 v17, v14, v19
	v_mov_b32_e32 v18, v25
	v_mov_b32_e32 v19, v4
	v_mov_b32_e32 v14, v11
	v_pk_mul_f32 v[14:15], v[18:19], v[14:15]
	v_mul_f32_e32 v5, 0x41800000, v5
	v_fma_f32 v14, v57, v2, v14
	v_mul_f32_e32 v10, 0x41800000, v10
	v_add_f32_e32 v14, v14, v15
	v_med3_f32 v5, v5, s78, v198
	v_med3_f32 v10, v10, s78, v198
	v_mul_f32_e32 v15, 0x41800000, v17
	v_mov_b32_e32 v17, v3
	v_cvt_pk_fp8_f32 v17, v5, v10
	v_mul_f32_e32 v14, 0x41800000, v14
	v_med3_f32 v15, v15, s78, v198
	v_med3_f32 v14, v14, s78, v198
	v_cvt_pk_fp8_f32 v17, v15, v14 op_sel:[0,0,1]
	v_lshlrev_b32_e32 v15, 16, v12
	v_mov_b32_e32 v14, v11
	v_permlane32_swap_b32_e32 v16, v17
	global_store_dwordx2 v[6:7], v[16:17], off offset:32
	v_mov_b32_e32 v16, v26
	v_mov_b32_e32 v17, v4
	v_pk_mul_f32 v[14:15], v[16:17], v[14:15]
	v_mov_b32_e32 v16, v27
	v_fma_f32 v5, v58, v2, v14
	v_add_f32_e32 v5, v5, v15
	v_and_b32_e32 v15, 0xffff0000, v12
	v_mov_b32_e32 v14, v11
	v_pk_mul_f32 v[14:15], v[16:17], v[14:15]
	v_mov_b32_e32 v16, v28
	v_fma_f32 v10, v59, v2, v14
	v_add_f32_e32 v10, v10, v15
	v_lshlrev_b32_e32 v15, 16, v13
	v_mov_b32_e32 v14, v11
	v_pk_mul_f32 v[14:15], v[16:17], v[14:15]
	v_and_b32_e32 v13, 0xffff0000, v13
	v_fma_f32 v12, v60, v2, v14
	v_add_f32_e32 v16, v12, v15
	v_mov_b32_e32 v14, v29
	v_mov_b32_e32 v15, v4
	v_mov_b32_e32 v12, v11
	v_pk_mul_f32 v[12:13], v[14:15], v[12:13]
	v_mul_f32_e32 v10, 0x41800000, v10
	v_fma_f32 v12, v61, v2, v12
	v_add_f32_e32 v12, v12, v13
	v_med3_f32 v13, v10, s78, v198
	v_mul_f32_e32 v10, 0x41800000, v16
	v_mul_f32_e32 v5, 0x41800000, v5
	v_med3_f32 v14, v10, s78, v198
	v_mul_f32_e32 v10, 0x41800000, v12
	v_med3_f32 v5, v5, s78, v198
	v_med3_f32 v12, v10, s78, v198
	v_mov_b32_e32 v10, v3
	v_cvt_pk_fp8_f32 v10, v5, v13
	v_lshlrev_b32_e32 v13, 16, v8
	v_cvt_pk_fp8_f32 v10, v14, v12 op_sel:[0,0,1]
	v_mov_b32_e32 v14, v30
	v_mov_b32_e32 v12, v11
	v_pk_mul_f32 v[12:13], v[14:15], v[12:13]
	v_mov_b32_e32 v14, v31
	v_fma_f32 v5, v62, v2, v12
	v_add_f32_e32 v16, v5, v13
	v_and_b32_e32 v13, 0xffff0000, v8
	v_mov_b32_e32 v12, v11
	v_pk_mul_f32 v[12:13], v[14:15], v[12:13]
	v_mov_b32_e32 v14, v32
	v_fma_f32 v5, v63, v2, v12
	v_add_f32_e32 v17, v5, v13
	v_lshlrev_b32_e32 v13, 16, v9
	v_mov_b32_e32 v12, v11
	v_pk_mul_f32 v[12:13], v[14:15], v[12:13]
	v_mov_b32_e32 v8, v33
	v_fma_f32 v5, v64, v2, v12
	v_add_f32_e32 v12, v5, v13
	v_and_b32_e32 v5, 0xffff0000, v9
	v_mov_b32_e32 v9, v4
	v_mov_b32_e32 v4, v11
	v_pk_mul_f32 v[4:5], v[8:9], v[4:5]
	v_mov_b32_e32 v11, v3
	v_fma_f32 v2, v65, v2, v4
	v_add_f32_e32 v2, v2, v5
	v_mul_f32_e32 v4, 0x41800000, v16
	v_mul_f32_e32 v5, 0x41800000, v17
	v_med3_f32 v4, v4, s78, v198
	v_med3_f32 v5, v5, s78, v198
	v_cvt_pk_fp8_f32 v11, v4, v5
	v_mul_f32_e32 v8, 0x41800000, v12
	v_mul_f32_e32 v2, 0x41800000, v2
	v_med3_f32 v8, v8, s78, v198
	v_med3_f32 v2, v2, s78, v198
	v_cvt_pk_fp8_f32 v11, v8, v2 op_sel:[0,0,1]
	s_nop 1
	v_permlane32_swap_b32_e32 v10, v11
	global_store_dwordx2 v[6:7], v[10:11], off offset:48
	s_waitcnt lgkmcnt(0)
	s_barrier
	s_cbranch_vccnz .LBB0_636
	s_cmpk_gt_i32 s14, 0xd7
	s_cbranch_scc0 .LBB0_708
	s_cmpk_lt_u32 s14, 0x138
	s_cselect_b64 s[4:5], -1, 0
	s_cmpk_gt_u32 s14, 0x137
	s_cbranch_scc0 .LBB0_709
	s_add_i32 s0, s14, 0xfffffe40
	s_cmpk_lt_u32 s0, 0x60
	s_cselect_b64 s[6:7], -1, 0
	s_cmpk_gt_u32 s0, 0x5f
	s_mov_b64 s[0:1], 0
	s_cbranch_scc0 .LBB0_713
	s_add_i32 s0, s14, 0xfffffde0
	s_cmp_gt_u32 s0, 0xffffff57
	s_cbranch_scc0 .LBB0_710
	s_cmpk_gt_u32 s14, 0x1b7
	s_mov_b64 s[0:1], -1
	s_cbranch_scc0 .LBB0_705
	s_load_dwordx2 s[0:1], s[48:49], 0x70
	s_add_i32 s2, s14, 0xfffffe48
	s_lshr_b32 s2, s2, 2
	s_add_i32 s82, s2, 2
	s_lshl_b64 s[2:3], s[82:83], 16
	s_waitcnt lgkmcnt(0)
	s_add_u32 s0, s0, s2
	s_addc_u32 s1, s1, s3
	s_lshl_b64 s[2:3], s[82:83], 15
	v_readlane_b32 s8, v254, 28
	s_add_u32 s2, s8, s2
	v_readlane_b32 s8, v254, 29
	v_mov_b32_e32 v21, v0
	s_addc_u32 s3, s8, s3
	s_lshl_b32 s8, s14, 6
	v_ashrrev_i32_e32 v20, 3, v21
	s_and_b32 s8, s8, 0xc0
	v_and_b32_e32 v2, -2, v20
	v_add_u32_e32 v4, s8, v2
	v_ashrrev_i32_e32 v5, 31, v4
	v_lshlrev_b64 v[6:7], 8, v[4:5]
	v_or_b32_e32 v4, 1, v4
	v_ashrrev_i32_e32 v5, 31, v4
	v_lshlrev_b64 v[4:5], 8, v[4:5]
	v_lshlrev_b32_e32 v22, 4, v21
	v_lshl_add_u64 v[12:13], s[0:1], 0, v[6:7]
	v_lshl_add_u64 v[16:17], s[0:1], 0, v[4:5]
	v_and_b32_e32 v2, 0xf0, v22
	v_lshl_add_u64 v[4:5], v[12:13], 0, v[2:3]
	v_lshl_add_u64 v[8:9], v[16:17], 0, v[2:3]
	global_load_dwordx4 v[4:7], v[4:5], off
	s_nop 0
	global_load_dwordx4 v[8:11], v[8:9], off
	s_nop 0
	global_load_dwordx4 v[12:15], v[12:13], off
	s_nop 0
	global_load_dwordx4 v[16:19], v[16:17], off
	v_lshlrev_b32_e32 v2, 9, v21
	v_ashrrev_i32_e32 v23, 6, v21
	v_and_b32_e32 v2, 0x1e00, v2
	v_bitop3_b32 v23, v23, v21, 7 bitop3:0x78
	v_lshrrev_b32_e32 v24, 2, v21
	v_add_u32_e32 v2, 0, v2
	v_lshlrev_b32_e32 v23, 4, v23
	v_and_b32_e32 v24, 12, v24
	s_barrier
	v_add3_u32 v2, v2, v23, v24
	s_waitcnt vmcnt(2)
	v_cvt_pk_bf16_f32 v4, v4, v8
	ds_write_b32 v2, v4
	v_cvt_pk_bf16_f32 v4, v5, v9
	ds_write_b32 v2, v4 offset:128
	v_cvt_pk_bf16_f32 v4, v6, v10
	ds_write_b32 v2, v4 offset:256
	v_cvt_pk_bf16_f32 v4, v7, v11
	ds_write_b32 v2, v4 offset:384
	s_waitcnt vmcnt(0)
	v_cvt_pk_bf16_f32 v4, v12, v16
	ds_write_b32 v2, v4 offset:8192
	v_cvt_pk_bf16_f32 v4, v13, v17
	ds_write_b32 v2, v4 offset:8320
	v_cvt_pk_bf16_f32 v4, v14, v18
	ds_write_b32 v2, v4 offset:8448
	v_cvt_pk_bf16_f32 v4, v15, v19
	ds_write_b32 v2, v4 offset:8576
	v_cvt_pk_bf16_f32 v4, v12, v16
	ds_write_b32 v2, v4 offset:16384
	v_cvt_pk_bf16_f32 v4, v13, v17
	ds_write_b32 v2, v4 offset:16512
	v_cvt_pk_bf16_f32 v4, v14, v18
	ds_write_b32 v2, v4 offset:16640
	v_cvt_pk_bf16_f32 v4, v15, v19
	ds_write_b32 v2, v4 offset:16768
	v_cvt_pk_bf16_f32 v4, v12, v16
	ds_write_b32 v2, v4 offset:24576
	v_cvt_pk_bf16_f32 v4, v13, v17
	ds_write_b32 v2, v4 offset:24704
	v_cvt_pk_bf16_f32 v4, v14, v18
	ds_write_b32 v2, v4 offset:24832
	v_cvt_pk_bf16_f32 v4, v15, v19
	ds_write_b32 v2, v4 offset:24960
	v_lshrrev_b32_e32 v4, 5, v21
	v_xor_b32_e32 v4, v4, v21
	v_lshlrev_b32_e32 v4, 4, v4
	v_lshlrev_b32_e32 v2, 7, v20
	v_and_b32_e32 v4, 0x70, v4
	v_add3_u32 v4, 0, v2, v4
	s_waitcnt lgkmcnt(0)
	s_barrier
	s_lshl_b32 s0, s8, 1
	ds_read_b128 v[4:7], v4
	s_add_u32 s0, s2, s0
	s_addc_u32 s1, s3, 0
	v_and_b32_e32 v2, 0x70, v22
	v_ashrrev_i32_e32 v21, 31, v20
	v_lshl_add_u64 v[8:9], s[0:1], 0, v[2:3]
	v_lshlrev_b64 v[10:11], 9, v[20:21]
	v_lshl_add_u64 v[8:9], v[8:9], 0, v[10:11]
	s_waitcnt lgkmcnt(0)
	global_store_dwordx4 v[8:9], v[4:7], off
	s_barrier
	s_mov_b64 s[0:1], 0
